# baseline (speedup 1.0000x reference)
.LBB1_13:
	v_mfma_f32_32x32x16_bf16 v[2:17], v[78:81], v[206:209], v[236:251]
	v_mfma_f32_32x32x16_bf16 v[2:17], v[74:77], v[190:193], v[2:17]
	ds_read_b128 v[174:177], v210
	v_add_u32_e32 v195, v230, v228
	ds_read_b128 v[170:173], v210 offset:1024
	v_exp_f32_e32 v199, v28
	v_exp_f32_e32 v198, v32
	v_exp_f32_e32 v197, v20
	v_exp_f32_e32 v196, v24
	v_mfma_f32_32x32x16_bf16 v[2:17], v[70:73], v[158:161], v[2:17]
	ds_read_b128 v[166:169], v210 offset:2048
	v_exp_f32_e32 v18, v18
	v_exp_f32_e32 v22, v22
	v_exp_f32_e32 v24, v26
	v_exp_f32_e32 v26, v30
	v_fma_f32 v20, v197, s12, s12
	v_fma_f32 v28, v196, s12, s12
	v_fma_f32 v30, v199, s12, s12
	v_fma_f32 v32, v198, s12, s12
	v_mfma_f32_32x32x16_bf16 v[2:17], v[66:69], v[142:145], v[2:17]
	ds_read_b128 v[162:165], v210 offset:3072
	v_exp_f32_e32 v19, v19
	v_exp_f32_e32 v23, v23
	v_exp_f32_e32 v27, v27
	v_exp_f32_e32 v31, v31
	v_fmac_f32_e32 v20, v18, v20
	v_fmac_f32_e32 v28, v22, v28
	v_fmac_f32_e32 v30, v24, v30
	v_fmac_f32_e32 v32, v26, v32
	v_mfma_f32_32x32x16_bf16 v[2:17], v[62:65], v[154:157], v[2:17]
	ds_read_b128 v[158:161], v210 offset:4096
	v_add_f32_e32 v22, 1.0, v19
	v_rcp_f32_e32 v19, v20
	v_rcp_f32_e32 v18, v28
	v_add_f32_e32 v20, 1.0, v23
	v_rcp_f32_e32 v191, v30
	v_rcp_f32_e32 v190, v32
	v_mfma_f32_32x32x16_bf16 v[2:17], v[58:61], v[182:185], v[2:17]
	ds_read_b128 v[154:157], v210 offset:5120
	v_exp_f32_e32 v206, v21
	v_exp_f32_e32 v207, v25
	v_add_f32_e32 v23, 1.0, v27
	v_rcp_f32_e32 v192, v20
	v_add_f32_e32 v20, 1.0, v31
	v_rcp_f32_e32 v193, v22
	v_mfma_f32_32x32x16_bf16 v[2:17], v[54:57], v[186:189], v[2:17]
	ds_read_b128 v[142:145], v210 offset:6144
	v_exp_f32_e32 v208, v29
	v_exp_f32_e32 v209, v33
	v_rcp_f32_e32 v183, v23
	v_rcp_f32_e32 v182, v20
	v_mfma_f32_32x32x16_bf16 v[2:17], v[50:53], v[134:137], v[2:17]
	ds_read_b128 v[130:133], v210 offset:7168
	v_fma_f32 v186, -v196, v18, v18
	v_fma_f32 v187, -v197, v19, v19
	ds_read_b128 v[18:21], v231 offset:36928
	ds_read_b128 v[22:25], v231 offset:36944
	ds_read_b128 v[26:29], v231 offset:36960
	ds_read_b128 v[30:33], v231 offset:36976
	v_pk_fma_f32 v[200:201], v[192:193], v[220:221], v[186:187]
	v_pk_fma_f32 v[134:135], v[198:199], v[190:191], v[190:191] neg_lo:[1,0,0] neg_hi:[1,0,0]
	s_nop 0
	v_pk_fma_f32 v[198:199], v[182:183], v[222:223], v[134:135]
	v_mfma_f32_32x32x16_bf16 v[2:17], v[46:49], v[138:141], v[2:17]
	ds_read_b128 v[134:137], v195 offset:16384
	v_add_f32_e32 v182, 1.0, v206
	v_exp_f32_e32 v183, v201
	v_exp_f32_e32 v186, v200
	v_exp_f32_e32 v187, v199
	v_exp_f32_e32 v188, v198
	v_add_f32_e32 v189, 1.0, v207
	v_add_f32_e32 v190, 1.0, v208
	v_add_f32_e32 v191, 1.0, v209
	v_mfma_f32_32x32x16_bf16 v[2:17], v[42:45], v[146:149], v[2:17]
	ds_read_b128 v[138:141], v195 offset:16416
	v_fmac_f32_e32 v182, v182, v183
	v_fmac_f32_e32 v189, v189, v186
	v_fmac_f32_e32 v190, v190, v187
	v_fmac_f32_e32 v191, v191, v188
	v_mfma_f32_32x32x16_bf16 v[2:17], v[38:41], v[150:153], v[2:17]
	ds_read_b128 v[146:149], v195 offset:16448
	v_rcp_f32_e32 v182, v182
	v_rcp_f32_e32 v189, v189
	v_mfma_f32_32x32x16_bf16 v[2:17], v[34:37], v[178:181], v[2:17]
	ds_read_b128 v[150:153], v195 offset:16480
	v_rcp_f32_e32 v190, v190
	v_rcp_f32_e32 v191, v191
	v_fma_f32 v182, -v183, v182, v182
	v_fma_f32 v183, -v186, v189, v189
	s_waitcnt lgkmcnt(4)
	v_mfma_f32_32x32x16_bf16 v[18:33], v[126:129], v[174:177], v[18:33]
	v_fma_f32 v186, -v187, v190, v190
	v_fma_f32 v187, -v188, v191, v191
	v_cvt_pk_bf16_f32 v252, v182, v183
	v_cvt_pk_bf16_f32 v253, v186, v187
	v_mfma_f32_32x32x16_bf16 v[18:33], v[122:125], v[170:173], v[18:33]
	s_nop 1
	v_exp_f32_e32 v179, v4
	v_exp_f32_e32 v178, v8
	v_exp_f32_e32 v181, v12
	v_exp_f32_e32 v180, v16
	v_mfma_f32_32x32x16_bf16 v[18:33], v[118:121], v[166:169], v[18:33]
	v_exp_f32_e32 v2, v2
	v_exp_f32_e32 v6, v6
	v_exp_f32_e32 v10, v10
	v_exp_f32_e32 v12, v14
	v_fma_f32 v4, v179, s12, s12
	v_fma_f32 v8, v178, s12, s12
	v_fma_f32 v14, v181, s12, s12
	v_fma_f32 v16, v180, s12, s12
	v_mfma_f32_32x32x16_bf16 v[18:33], v[114:117], v[162:165], v[18:33]
	v_exp_f32_e32 v3, v3
	v_fmac_f32_e32 v4, v2, v4
	v_exp_f32_e32 v2, v7
	v_fmac_f32_e32 v8, v6, v8
	v_exp_f32_e32 v6, v11
	v_exp_f32_e32 v7, v15
	v_fmac_f32_e32 v14, v10, v14
	v_fmac_f32_e32 v16, v12, v16
	v_mfma_f32_32x32x16_bf16 v[18:33], v[110:113], v[158:161], v[18:33]
	v_add_f32_e32 v10, 1.0, v3
	v_rcp_f32_e32 v3, v4
	v_add_f32_e32 v4, 1.0, v2
	v_rcp_f32_e32 v2, v8
	v_rcp_f32_e32 v183, v14
	v_rcp_f32_e32 v182, v16
	v_mfma_f32_32x32x16_bf16 v[18:33], v[106:109], v[154:157], v[18:33]
	v_add_f32_e32 v6, 1.0, v6
	v_add_f32_e32 v7, 1.0, v7
	v_rcp_f32_e32 v187, v10
	v_rcp_f32_e32 v186, v4
	v_exp_f32_e32 v190, v5
	v_exp_f32_e32 v191, v9
	v_mfma_f32_32x32x16_bf16 v[18:33], v[102:105], v[142:145], v[18:33]
	v_rcp_f32_e32 v189, v6
	v_rcp_f32_e32 v188, v7
	v_exp_f32_e32 v192, v13
	v_exp_f32_e32 v193, v17
	v_mfma_f32_32x32x16_bf16 v[18:33], v[98:101], v[130:133], v[18:33]
	v_fma_f32 v178, -v178, v2, v2
	v_fma_f32 v179, -v179, v3, v3
	v_pk_fma_f32 v[206:207], v[186:187], v[216:217], v[178:179]
	s_nop 0
	v_pk_fma_f32 v[178:179], v[180:181], v[182:183], v[182:183] neg_lo:[1,0,0] neg_hi:[1,0,0]
	s_nop 0
	v_pk_fma_f32 v[208:209], v[188:189], v[218:219], v[178:179]
	s_waitcnt lgkmcnt(0)
	v_mfma_f32_32x32x16_bf16 v[18:33], v[94:97], v[134:137], v[18:33]
	v_add_f32_e32 v178, 1.0, v190
	v_exp_f32_e32 v179, v207
	v_add_f32_e32 v180, 1.0, v191
	v_exp_f32_e32 v181, v206
	v_exp_f32_e32 v182, v209
	v_exp_f32_e32 v183, v208
	v_add_f32_e32 v184, 1.0, v192
	v_add_f32_e32 v185, 1.0, v193
	v_mfma_f32_32x32x16_bf16 v[18:33], v[90:93], v[138:141], v[18:33]
	v_fmac_f32_e32 v178, v178, v179
	v_fmac_f32_e32 v180, v180, v181
	v_fmac_f32_e32 v184, v184, v182
	v_fmac_f32_e32 v185, v185, v183
	v_mfma_f32_32x32x16_bf16 v[18:33], v[86:89], v[146:149], v[18:33]
	v_rcp_f32_e32 v178, v178
	v_rcp_f32_e32 v180, v180
	v_rcp_f32_e32 v184, v184
	v_rcp_f32_e32 v185, v185
	v_mfma_f32_32x32x16_bf16 v[18:33], v[82:85], v[150:153], v[18:33]
	v_fma_f32 v178, -v179, v178, v178
	v_fma_f32 v179, -v181, v180, v180
	v_fma_f32 v180, -v182, v184, v184
	v_fma_f32 v181, -v183, v185, v185
	v_cvt_pk_bf16_f32 v254, v178, v179
	v_cvt_pk_bf16_f32 v255, v180, v181
	ds_write_b128 v211, v[252:255] offset:8192
	s_waitcnt lgkmcnt(0)
	s_barrier
	s_add_i32 s1, s1, 2
	s_cmp_gt_u32 s1, 16
	v_add_u32_e32 v232, 0x200, v232
	s_cbranch_scc1 .LBB1_30
.LBB1_14:
	v_mfma_f32_32x32x16_bf16 v[2:17], v[78:81], v[174:177], v[236:251]
	v_mfma_f32_32x32x16_bf16 v[2:17], v[74:77], v[170:173], v[2:17]
	v_add_u32_e32 v192, v230, v229
	ds_read2_b32 v[228:229], v232 offset1:32
	ds_read_b128 v[194:197], v210 offset:8192
	ds_read_b128 v[178:181], v210 offset:9216
	v_exp_f32_e32 v187, v20
	v_exp_f32_e32 v186, v24
	v_exp_f32_e32 v189, v28
	v_exp_f32_e32 v188, v32
	v_mfma_f32_32x32x16_bf16 v[2:17], v[70:73], v[166:169], v[2:17]
	ds_read_b128 v[170:173], v210 offset:10240
	v_exp_f32_e32 v18, v18
	v_exp_f32_e32 v22, v22
	v_exp_f32_e32 v24, v26
	v_exp_f32_e32 v26, v30
	v_fma_f32 v20, v187, s12, s12
	v_fma_f32 v28, v186, s12, s12
	v_fma_f32 v30, v189, s12, s12
	v_fma_f32 v32, v188, s12, s12
	v_mfma_f32_32x32x16_bf16 v[2:17], v[66:69], v[162:165], v[2:17]
	ds_read_b128 v[166:169], v210 offset:11264
	v_exp_f32_e32 v19, v19
	v_exp_f32_e32 v23, v23
	v_exp_f32_e32 v27, v27
	v_exp_f32_e32 v31, v31
	v_fmac_f32_e32 v20, v18, v20
	v_fmac_f32_e32 v28, v22, v28
	v_fmac_f32_e32 v30, v24, v30
	v_fmac_f32_e32 v32, v26, v32
	v_mfma_f32_32x32x16_bf16 v[2:17], v[62:65], v[158:161], v[2:17]
	ds_read_b128 v[162:165], v210 offset:12288
	v_add_f32_e32 v22, 1.0, v19
	v_rcp_f32_e32 v19, v20
	v_rcp_f32_e32 v18, v28
	v_rcp_f32_e32 v191, v30
	v_rcp_f32_e32 v190, v32
	v_add_f32_e32 v20, 1.0, v23
	v_mfma_f32_32x32x16_bf16 v[2:17], v[58:61], v[154:157], v[2:17]
	ds_read_b128 v[174:177], v210 offset:13312
	v_rcp_f32_e32 v159, v22
	v_rcp_f32_e32 v158, v20
	v_exp_f32_e32 v160, v21
	v_exp_f32_e32 v161, v25
	v_add_f32_e32 v23, 1.0, v27
	v_add_f32_e32 v20, 1.0, v31
	v_mfma_f32_32x32x16_bf16 v[2:17], v[54:57], v[142:145], v[2:17]
	ds_read_b128 v[182:185], v210 offset:14336
	v_rcp_f32_e32 v155, v23
	v_rcp_f32_e32 v154, v20
	v_exp_f32_e32 v193, v29
	v_exp_f32_e32 v217, v33
	v_mfma_f32_32x32x16_bf16 v[2:17], v[50:53], v[130:133], v[2:17]
	ds_read_b128 v[142:145], v210 offset:15360
	v_fma_f32 v156, -v186, v18, v18
	v_fma_f32 v157, -v187, v19, v19
	ds_read_b128 v[18:21], v231 offset:36928
	ds_read_b128 v[22:25], v231 offset:36944
	ds_read_b128 v[26:29], v231 offset:36960
	ds_read_b128 v[30:33], v231 offset:36976
	v_pk_fma_f32 v[214:215], v[158:159], v[214:215], v[156:157]
	v_pk_fma_f32 v[130:131], v[188:189], v[190:191], v[190:191] neg_lo:[1,0,0] neg_hi:[1,0,0]
	s_nop 0
	v_pk_fma_f32 v[212:213], v[154:155], v[212:213], v[130:131]
	v_mfma_f32_32x32x16_bf16 v[2:17], v[46:49], v[134:137], v[2:17]
	ds_read_b128 v[154:157], v192 offset:16384
	v_add_f32_e32 v130, 1.0, v160
	v_exp_f32_e32 v131, v215
	v_exp_f32_e32 v132, v214
	v_exp_f32_e32 v133, v213
	v_exp_f32_e32 v220, v212
	v_add_f32_e32 v134, 1.0, v161
	v_add_f32_e32 v135, 1.0, v193
	v_add_f32_e32 v136, 1.0, v217
	v_mfma_f32_32x32x16_bf16 v[2:17], v[42:45], v[138:141], v[2:17]
	ds_read_b128 v[158:161], v192 offset:16416
	v_fmac_f32_e32 v130, v130, v131
	v_fmac_f32_e32 v134, v134, v132
	v_fmac_f32_e32 v135, v135, v133
	v_fmac_f32_e32 v136, v136, v220
	v_mfma_f32_32x32x16_bf16 v[2:17], v[38:41], v[146:149], v[2:17]
	ds_read_b128 v[186:189], v192 offset:16448
	v_rcp_f32_e32 v130, v130
	v_rcp_f32_e32 v134, v134
	v_mfma_f32_32x32x16_bf16 v[2:17], v[34:37], v[150:153], v[2:17]
	ds_read_b128 v[190:193], v192 offset:16480
	v_rcp_f32_e32 v135, v135
	v_rcp_f32_e32 v136, v136
	v_fma_f32 v130, -v131, v130, v130
	v_fma_f32 v131, -v132, v134, v134
	s_waitcnt lgkmcnt(4)
	v_mfma_f32_32x32x16_bf16 v[18:33], v[126:129], v[194:197], v[18:33]
	v_fma_f32 v132, -v133, v135, v135
	v_fma_f32 v133, -v220, v136, v136
	v_cvt_pk_bf16_f32 v252, v130, v131
	v_cvt_pk_bf16_f32 v253, v132, v133
	v_mfma_f32_32x32x16_bf16 v[18:33], v[122:125], v[178:181], v[18:33]
	s_nop 1
	v_exp_f32_e32 v131, v4
	v_exp_f32_e32 v130, v8
	v_exp_f32_e32 v133, v12
	v_exp_f32_e32 v132, v16
	v_mfma_f32_32x32x16_bf16 v[18:33], v[118:121], v[170:173], v[18:33]
	v_exp_f32_e32 v2, v2
	v_exp_f32_e32 v6, v6
	v_exp_f32_e32 v10, v10
	v_exp_f32_e32 v12, v14
	v_fma_f32 v4, v131, s12, s12
	v_fma_f32 v8, v130, s12, s12
	v_fma_f32 v14, v133, s12, s12
	v_fma_f32 v16, v132, s12, s12
	v_mfma_f32_32x32x16_bf16 v[18:33], v[114:117], v[166:169], v[18:33]
	v_exp_f32_e32 v3, v3
	v_fmac_f32_e32 v4, v2, v4
	v_exp_f32_e32 v2, v7
	v_fmac_f32_e32 v8, v6, v8
	v_exp_f32_e32 v6, v11
	v_exp_f32_e32 v7, v15
	v_fmac_f32_e32 v14, v10, v14
	v_fmac_f32_e32 v16, v12, v16
	v_mfma_f32_32x32x16_bf16 v[18:33], v[110:113], v[162:165], v[18:33]
	v_add_f32_e32 v10, 1.0, v3
	v_rcp_f32_e32 v3, v4
	v_add_f32_e32 v4, 1.0, v2
	v_rcp_f32_e32 v2, v8
	v_rcp_f32_e32 v135, v14
	v_rcp_f32_e32 v134, v16
	v_mfma_f32_32x32x16_bf16 v[18:33], v[106:109], v[174:177], v[18:33]
	v_add_f32_e32 v6, 1.0, v6
	v_add_f32_e32 v7, 1.0, v7
	v_rcp_f32_e32 v137, v10
	v_rcp_f32_e32 v136, v4
	v_exp_f32_e32 v140, v5
	v_exp_f32_e32 v141, v9
	v_mfma_f32_32x32x16_bf16 v[18:33], v[102:105], v[182:185], v[18:33]
	v_rcp_f32_e32 v139, v6
	v_rcp_f32_e32 v138, v7
	v_exp_f32_e32 v146, v13
	v_exp_f32_e32 v147, v17
	v_mfma_f32_32x32x16_bf16 v[18:33], v[98:101], v[142:145], v[18:33]
	v_fma_f32 v130, -v130, v2, v2
	v_fma_f32 v131, -v131, v3, v3
	v_pk_fma_f32 v[224:225], v[136:137], v[204:205], v[130:131]
	s_nop 0
	v_pk_fma_f32 v[130:131], v[132:133], v[134:135], v[134:135] neg_lo:[1,0,0] neg_hi:[1,0,0]
	s_nop 0
	v_pk_fma_f32 v[226:227], v[138:139], v[202:203], v[130:131]
	s_waitcnt lgkmcnt(0)
	v_mfma_f32_32x32x16_bf16 v[18:33], v[94:97], v[154:157], v[18:33]
	v_add_f32_e32 v130, 1.0, v140
	v_exp_f32_e32 v131, v225
	v_add_f32_e32 v132, 1.0, v141
	v_exp_f32_e32 v133, v224
	v_exp_f32_e32 v134, v227
	v_exp_f32_e32 v135, v226
	v_add_f32_e32 v136, 1.0, v146
	v_add_f32_e32 v137, 1.0, v147
	v_mfma_f32_32x32x16_bf16 v[18:33], v[90:93], v[158:161], v[18:33]
	v_fmac_f32_e32 v130, v130, v131
	v_fmac_f32_e32 v132, v132, v133
	v_fmac_f32_e32 v136, v136, v134
	v_fmac_f32_e32 v137, v137, v135
	v_mfma_f32_32x32x16_bf16 v[18:33], v[86:89], v[186:189], v[18:33]
	v_rcp_f32_e32 v130, v130
	v_rcp_f32_e32 v132, v132
	v_rcp_f32_e32 v136, v136
	v_rcp_f32_e32 v137, v137
	v_mfma_f32_32x32x16_bf16 v[18:33], v[82:85], v[190:193], v[18:33]
	v_fma_f32 v130, -v131, v130, v130
	v_fma_f32 v131, -v133, v132, v132
	v_fma_f32 v132, -v134, v136, v136
	v_fma_f32 v133, -v135, v137, v137
	v_cvt_pk_bf16_f32 v254, v130, v131
	v_cvt_pk_bf16_f32 v255, v132, v133
	ds_write_b128 v211, v[252:255] offset:0
	s_waitcnt lgkmcnt(0)
	s_barrier
	v_mfma_f32_32x32x16_bf16 v[2:17], v[78:81], v[194:197], v[236:251]
	v_mfma_f32_32x32x16_bf16 v[2:17], v[74:77], v[178:181], v[2:17]
	ds_read_b128 v[202:205], v210
	v_add_u32_e32 v216, v230, v228
	ds_read_b128 v[194:197], v210 offset:1024
	v_exp_f32_e32 v147, v20
	v_exp_f32_e32 v146, v24
	v_exp_f32_e32 v149, v28
	v_exp_f32_e32 v148, v32
	v_mfma_f32_32x32x16_bf16 v[2:17], v[70:73], v[170:173], v[2:17]
	ds_read_b128 v[138:141], v210 offset:2048
	v_exp_f32_e32 v18, v18
	v_exp_f32_e32 v22, v22
	v_exp_f32_e32 v24, v26
	v_exp_f32_e32 v26, v30
	v_fma_f32 v20, v147, s12, s12
	v_fma_f32 v28, v146, s12, s12
	v_fma_f32 v30, v149, s12, s12
	v_fma_f32 v32, v148, s12, s12
	v_mfma_f32_32x32x16_bf16 v[2:17], v[66:69], v[166:169], v[2:17]
	ds_read_b128 v[134:137], v210 offset:3072
	v_exp_f32_e32 v19, v19
	v_exp_f32_e32 v23, v23
	v_exp_f32_e32 v27, v27
	v_exp_f32_e32 v31, v31
	v_fmac_f32_e32 v20, v18, v20
	v_fmac_f32_e32 v28, v22, v28
	v_fmac_f32_e32 v30, v24, v30
	v_fmac_f32_e32 v32, v26, v32
	v_mfma_f32_32x32x16_bf16 v[2:17], v[62:65], v[162:165], v[2:17]
	ds_read_b128 v[166:169], v210 offset:4096
	v_add_f32_e32 v22, 1.0, v19
	v_rcp_f32_e32 v19, v20
	v_rcp_f32_e32 v18, v28
	v_rcp_f32_e32 v151, v30
	v_rcp_f32_e32 v150, v32
	v_add_f32_e32 v20, 1.0, v23
	v_mfma_f32_32x32x16_bf16 v[2:17], v[58:61], v[174:177], v[2:17]
	ds_read_b128 v[162:165], v210 offset:5120
	v_rcp_f32_e32 v153, v22
	v_rcp_f32_e32 v152, v20
	v_add_f32_e32 v23, 1.0, v27
	v_add_f32_e32 v20, 1.0, v31
	v_exp_f32_e32 v180, v21
	v_exp_f32_e32 v181, v25
	v_mfma_f32_32x32x16_bf16 v[2:17], v[54:57], v[182:185], v[2:17]
	ds_read_b128 v[170:173], v210 offset:6144
	v_rcp_f32_e32 v175, v23
	v_rcp_f32_e32 v174, v20
	v_exp_f32_e32 v176, v29
	v_exp_f32_e32 v177, v33
	v_mfma_f32_32x32x16_bf16 v[2:17], v[50:53], v[142:145], v[2:17]
	ds_read_b128 v[130:133], v210 offset:7168
	v_fma_f32 v146, -v146, v18, v18
	v_fma_f32 v147, -v147, v19, v19
	ds_read_b128 v[18:21], v231 offset:36928
	ds_read_b128 v[22:25], v231 offset:36944
	ds_read_b128 v[26:29], v231 offset:36960
	ds_read_b128 v[30:33], v231 offset:36976
	v_pk_fma_f32 v[220:221], v[152:153], v[200:201], v[146:147]
	v_pk_fma_f32 v[142:143], v[148:149], v[150:151], v[150:151] neg_lo:[1,0,0] neg_hi:[1,0,0]
	s_nop 0
	v_pk_fma_f32 v[222:223], v[174:175], v[198:199], v[142:143]
	v_mfma_f32_32x32x16_bf16 v[2:17], v[46:49], v[154:157], v[2:17]
	ds_read_b128 v[146:149], v216 offset:16384
	v_add_f32_e32 v142, 1.0, v180
	v_exp_f32_e32 v143, v221
	v_exp_f32_e32 v144, v220
	v_exp_f32_e32 v145, v223
	v_exp_f32_e32 v180, v222
	v_add_f32_e32 v154, 1.0, v181
	v_add_f32_e32 v155, 1.0, v176
	v_add_f32_e32 v156, 1.0, v177
	v_mfma_f32_32x32x16_bf16 v[2:17], v[42:45], v[158:161], v[2:17]
	ds_read_b128 v[150:153], v216 offset:16416
	v_fmac_f32_e32 v142, v142, v143
	v_fmac_f32_e32 v154, v154, v144
	v_fmac_f32_e32 v155, v155, v145
	v_fmac_f32_e32 v156, v156, v180
	v_mfma_f32_32x32x16_bf16 v[2:17], v[38:41], v[186:189], v[2:17]
	ds_read_b128 v[174:177], v216 offset:16448
	v_rcp_f32_e32 v142, v142
	v_rcp_f32_e32 v154, v154
	v_mfma_f32_32x32x16_bf16 v[2:17], v[34:37], v[190:193], v[2:17]
	ds_read_b128 v[198:201], v216 offset:16480
	v_rcp_f32_e32 v155, v155
	v_rcp_f32_e32 v156, v156
	v_fma_f32 v142, -v143, v142, v142
	v_fma_f32 v143, -v144, v154, v154
	s_waitcnt lgkmcnt(4)
	v_mfma_f32_32x32x16_bf16 v[18:33], v[126:129], v[202:205], v[18:33]
	v_fma_f32 v144, -v145, v155, v155
	v_fma_f32 v145, -v180, v156, v156
	v_cvt_pk_bf16_f32 v252, v142, v143
	v_cvt_pk_bf16_f32 v253, v144, v145
	v_mfma_f32_32x32x16_bf16 v[18:33], v[122:125], v[194:197], v[18:33]
	s_nop 1
	v_exp_f32_e32 v143, v4
	v_exp_f32_e32 v142, v8
	v_exp_f32_e32 v145, v12
	v_exp_f32_e32 v144, v16
	v_mfma_f32_32x32x16_bf16 v[18:33], v[118:121], v[138:141], v[18:33]
	v_exp_f32_e32 v2, v2
	v_exp_f32_e32 v6, v6
	v_exp_f32_e32 v10, v10
	v_exp_f32_e32 v12, v14
	v_fma_f32 v4, v143, s12, s12
	v_fma_f32 v8, v142, s12, s12
	v_fma_f32 v14, v145, s12, s12
	v_fma_f32 v16, v144, s12, s12
	v_mfma_f32_32x32x16_bf16 v[18:33], v[114:117], v[134:137], v[18:33]
	v_exp_f32_e32 v3, v3
	v_fmac_f32_e32 v4, v2, v4
	v_exp_f32_e32 v2, v7
	v_fmac_f32_e32 v8, v6, v8
	v_exp_f32_e32 v6, v11
	v_exp_f32_e32 v7, v15
	v_fmac_f32_e32 v14, v10, v14
	v_fmac_f32_e32 v16, v12, v16
	v_mfma_f32_32x32x16_bf16 v[18:33], v[110:113], v[166:169], v[18:33]
	v_add_f32_e32 v10, 1.0, v3
	v_rcp_f32_e32 v3, v4
	v_add_f32_e32 v4, 1.0, v2
	v_rcp_f32_e32 v2, v8
	v_rcp_f32_e32 v155, v14
	v_rcp_f32_e32 v154, v16
	v_mfma_f32_32x32x16_bf16 v[18:33], v[106:109], v[162:165], v[18:33]
	v_add_f32_e32 v6, 1.0, v6
	v_add_f32_e32 v7, 1.0, v7
	v_rcp_f32_e32 v157, v10
	v_rcp_f32_e32 v156, v4
	v_exp_f32_e32 v160, v5
	v_exp_f32_e32 v161, v9
	v_mfma_f32_32x32x16_bf16 v[18:33], v[102:105], v[170:173], v[18:33]
	v_rcp_f32_e32 v159, v6
	v_rcp_f32_e32 v158, v7
	v_exp_f32_e32 v180, v13
	v_exp_f32_e32 v181, v17
	v_mfma_f32_32x32x16_bf16 v[18:33], v[98:101], v[130:133], v[18:33]
	v_fma_f32 v142, -v142, v2, v2
	v_fma_f32 v143, -v143, v3, v3
	v_pk_fma_f32 v[216:217], v[156:157], v[206:207], v[142:143]
	s_nop 0
	v_pk_fma_f32 v[142:143], v[144:145], v[154:155], v[154:155] neg_lo:[1,0,0] neg_hi:[1,0,0]
	s_nop 0
	v_pk_fma_f32 v[218:219], v[158:159], v[208:209], v[142:143]
	s_waitcnt lgkmcnt(0)
	v_mfma_f32_32x32x16_bf16 v[18:33], v[94:97], v[146:149], v[18:33]
	v_add_f32_e32 v142, 1.0, v160
	v_exp_f32_e32 v143, v217
	v_add_f32_e32 v144, 1.0, v161
	v_exp_f32_e32 v145, v216
	v_exp_f32_e32 v154, v219
	v_exp_f32_e32 v155, v218
	v_add_f32_e32 v156, 1.0, v180
	v_add_f32_e32 v157, 1.0, v181
	v_mfma_f32_32x32x16_bf16 v[18:33], v[90:93], v[150:153], v[18:33]
	v_fmac_f32_e32 v142, v142, v143
	v_fmac_f32_e32 v144, v144, v145
	v_fmac_f32_e32 v156, v156, v154
	v_fmac_f32_e32 v157, v157, v155
	v_mfma_f32_32x32x16_bf16 v[18:33], v[86:89], v[174:177], v[18:33]
	v_rcp_f32_e32 v142, v142
	v_rcp_f32_e32 v144, v144
	v_rcp_f32_e32 v156, v156
	v_rcp_f32_e32 v157, v157
	v_mfma_f32_32x32x16_bf16 v[18:33], v[82:85], v[198:201], v[18:33]
	v_fma_f32 v142, -v143, v142, v142
	v_fma_f32 v143, -v145, v144, v144
	v_fma_f32 v144, -v154, v156, v156
	v_fma_f32 v145, -v155, v157, v157
	v_cvt_pk_bf16_f32 v254, v142, v143
	v_cvt_pk_bf16_f32 v255, v144, v145
	ds_write_b128 v211, v[252:255] offset:8192
	s_waitcnt lgkmcnt(0)
	s_barrier
	v_mfma_f32_32x32x16_bf16 v[2:17], v[78:81], v[202:205], v[236:251]
	v_mfma_f32_32x32x16_bf16 v[2:17], v[74:77], v[194:197], v[2:17]
	v_add_u32_e32 v234, v230, v229
	ds_read2_b32 v[228:229], v232 offset0:64 offset1:96
	ds_read_b128 v[206:209], v210 offset:8192
	ds_read_b128 v[190:193], v210 offset:9216
	v_exp_f32_e32 v179, v20
	v_exp_f32_e32 v178, v24
	v_exp_f32_e32 v181, v28
	v_exp_f32_e32 v180, v32
	v_mfma_f32_32x32x16_bf16 v[2:17], v[70:73], v[138:141], v[2:17]
	ds_read_b128 v[158:161], v210 offset:10240
	v_exp_f32_e32 v18, v18
	v_exp_f32_e32 v22, v22
	v_exp_f32_e32 v24, v26
	v_exp_f32_e32 v26, v30
	v_fma_f32 v20, v179, s12, s12
	v_fma_f32 v28, v178, s12, s12
	v_fma_f32 v30, v181, s12, s12
	v_fma_f32 v32, v180, s12, s12
	v_mfma_f32_32x32x16_bf16 v[2:17], v[66:69], v[134:137], v[2:17]
	ds_read_b128 v[142:145], v210 offset:11264
	v_exp_f32_e32 v19, v19
	v_exp_f32_e32 v23, v23
	v_exp_f32_e32 v27, v27
	v_exp_f32_e32 v31, v31
	v_fmac_f32_e32 v20, v18, v20
	v_fmac_f32_e32 v28, v22, v28
	v_fmac_f32_e32 v30, v24, v30
	v_fmac_f32_e32 v32, v26, v32
	v_mfma_f32_32x32x16_bf16 v[2:17], v[62:65], v[166:169], v[2:17]
	ds_read_b128 v[154:157], v210 offset:12288
	v_add_f32_e32 v22, 1.0, v19
	v_rcp_f32_e32 v19, v20
	v_rcp_f32_e32 v18, v28
	v_rcp_f32_e32 v139, v30
	v_rcp_f32_e32 v138, v32
	v_add_f32_e32 v20, 1.0, v23
	v_mfma_f32_32x32x16_bf16 v[2:17], v[58:61], v[162:165], v[2:17]
	ds_read_b128 v[182:185], v210 offset:13312
	v_rcp_f32_e32 v141, v22
	v_rcp_f32_e32 v140, v20
	v_add_f32_e32 v23, 1.0, v27
	v_add_f32_e32 v20, 1.0, v31
	v_exp_f32_e32 v168, v21
	v_exp_f32_e32 v169, v25
	v_mfma_f32_32x32x16_bf16 v[2:17], v[54:57], v[170:173], v[2:17]
	ds_read_b128 v[186:189], v210 offset:14336
	v_rcp_f32_e32 v163, v23
	v_rcp_f32_e32 v162, v20
	v_exp_f32_e32 v194, v29
	v_exp_f32_e32 v195, v33
	v_mfma_f32_32x32x16_bf16 v[2:17], v[50:53], v[130:133], v[2:17]
	ds_read_b128 v[134:137], v210 offset:15360
	v_fma_f32 v166, -v178, v18, v18
	v_fma_f32 v167, -v179, v19, v19
	ds_read_b128 v[18:21], v231 offset:36928
	ds_read_b128 v[22:25], v231 offset:36944
	ds_read_b128 v[26:29], v231 offset:36960
	ds_read_b128 v[30:33], v231 offset:36976
	v_pk_fma_f32 v[214:215], v[140:141], v[214:215], v[166:167]
	v_pk_fma_f32 v[130:131], v[180:181], v[138:139], v[138:139] neg_lo:[1,0,0] neg_hi:[1,0,0]
	s_nop 0
	v_pk_fma_f32 v[212:213], v[162:163], v[212:213], v[130:131]
	v_mfma_f32_32x32x16_bf16 v[2:17], v[46:49], v[146:149], v[2:17]
	ds_read_b128 v[138:141], v234 offset:16384
	v_add_f32_e32 v130, 1.0, v168
	v_exp_f32_e32 v131, v215
	v_exp_f32_e32 v132, v214
	v_exp_f32_e32 v133, v213
	v_exp_f32_e32 v162, v212
	v_add_f32_e32 v163, 1.0, v169
	v_add_f32_e32 v166, 1.0, v194
	v_add_f32_e32 v167, 1.0, v195
	v_mfma_f32_32x32x16_bf16 v[2:17], v[42:45], v[150:153], v[2:17]
	ds_read_b128 v[146:149], v234 offset:16416
	v_fmac_f32_e32 v130, v130, v131
	v_fmac_f32_e32 v163, v163, v132
	v_fmac_f32_e32 v166, v166, v133
	v_fmac_f32_e32 v167, v167, v162
	v_mfma_f32_32x32x16_bf16 v[2:17], v[38:41], v[174:177], v[2:17]
	ds_read_b128 v[150:153], v234 offset:16448
	v_rcp_f32_e32 v130, v130
	v_rcp_f32_e32 v163, v163
	v_mfma_f32_32x32x16_bf16 v[2:17], v[34:37], v[198:201], v[2:17]
	ds_read_b128 v[178:181], v234 offset:16480
	v_rcp_f32_e32 v166, v166
	v_rcp_f32_e32 v167, v167
	v_fma_f32 v130, -v131, v130, v130
	v_fma_f32 v131, -v132, v163, v163
	s_waitcnt lgkmcnt(4)
	v_mfma_f32_32x32x16_bf16 v[18:33], v[126:129], v[206:209], v[18:33]
	v_fma_f32 v132, -v133, v166, v166
	v_fma_f32 v133, -v162, v167, v167
	v_cvt_pk_bf16_f32 v252, v130, v131
	v_cvt_pk_bf16_f32 v253, v132, v133
	v_mfma_f32_32x32x16_bf16 v[18:33], v[122:125], v[190:193], v[18:33]
	s_nop 1
	v_exp_f32_e32 v131, v4
	v_exp_f32_e32 v130, v8
	v_exp_f32_e32 v133, v12
	v_exp_f32_e32 v132, v16
	v_mfma_f32_32x32x16_bf16 v[18:33], v[118:121], v[158:161], v[18:33]
	v_exp_f32_e32 v2, v2
	v_exp_f32_e32 v6, v6
	v_exp_f32_e32 v10, v10
	v_exp_f32_e32 v12, v14
	v_fma_f32 v4, v131, s12, s12
	v_fma_f32 v8, v130, s12, s12
	v_fma_f32 v14, v133, s12, s12
	v_fma_f32 v16, v132, s12, s12
	v_mfma_f32_32x32x16_bf16 v[18:33], v[114:117], v[142:145], v[18:33]
	v_exp_f32_e32 v3, v3
	v_fmac_f32_e32 v4, v2, v4
	v_exp_f32_e32 v2, v7
	v_fmac_f32_e32 v8, v6, v8
	v_exp_f32_e32 v6, v11
	v_exp_f32_e32 v7, v15
	v_fmac_f32_e32 v14, v10, v14
	v_fmac_f32_e32 v16, v12, v16
	v_mfma_f32_32x32x16_bf16 v[18:33], v[110:113], v[154:157], v[18:33]
	v_add_f32_e32 v10, 1.0, v3
	v_rcp_f32_e32 v3, v4
	v_add_f32_e32 v4, 1.0, v2
	v_rcp_f32_e32 v2, v8
	v_rcp_f32_e32 v163, v14
	v_rcp_f32_e32 v162, v16
	v_mfma_f32_32x32x16_bf16 v[18:33], v[106:109], v[182:185], v[18:33]
	v_add_f32_e32 v6, 1.0, v6
	v_add_f32_e32 v7, 1.0, v7
	v_rcp_f32_e32 v167, v10
	v_rcp_f32_e32 v166, v4
	v_exp_f32_e32 v170, v5
	v_exp_f32_e32 v171, v9
	v_mfma_f32_32x32x16_bf16 v[18:33], v[102:105], v[186:189], v[18:33]
	v_rcp_f32_e32 v169, v6
	v_rcp_f32_e32 v168, v7
	v_exp_f32_e32 v172, v13
	v_exp_f32_e32 v173, v17
	v_mfma_f32_32x32x16_bf16 v[18:33], v[98:101], v[134:137], v[18:33]
	v_fma_f32 v130, -v130, v2, v2
	v_fma_f32 v131, -v131, v3, v3
	v_pk_fma_f32 v[204:205], v[166:167], v[224:225], v[130:131]
	s_nop 0
	v_pk_fma_f32 v[130:131], v[132:133], v[162:163], v[162:163] neg_lo:[1,0,0] neg_hi:[1,0,0]
	s_nop 0
	v_pk_fma_f32 v[202:203], v[168:169], v[226:227], v[130:131]
	s_waitcnt lgkmcnt(0)
	v_mfma_f32_32x32x16_bf16 v[18:33], v[94:97], v[138:141], v[18:33]
	v_add_f32_e32 v130, 1.0, v170
	v_exp_f32_e32 v131, v205
	v_add_f32_e32 v132, 1.0, v171
	v_exp_f32_e32 v133, v204
	v_exp_f32_e32 v162, v203
	v_exp_f32_e32 v163, v202
	v_add_f32_e32 v164, 1.0, v172
	v_add_f32_e32 v165, 1.0, v173
	v_mfma_f32_32x32x16_bf16 v[18:33], v[90:93], v[146:149], v[18:33]
	v_fmac_f32_e32 v130, v130, v131
	v_fmac_f32_e32 v132, v132, v133
	v_fmac_f32_e32 v164, v164, v162
	v_fmac_f32_e32 v165, v165, v163
	v_mfma_f32_32x32x16_bf16 v[18:33], v[86:89], v[150:153], v[18:33]
	v_rcp_f32_e32 v130, v130
	v_rcp_f32_e32 v132, v132
	v_rcp_f32_e32 v164, v164
	v_rcp_f32_e32 v165, v165
	v_mfma_f32_32x32x16_bf16 v[18:33], v[82:85], v[178:181], v[18:33]
	v_fma_f32 v130, -v131, v130, v130
	v_fma_f32 v131, -v133, v132, v132
	v_fma_f32 v132, -v162, v164, v164
	v_fma_f32 v133, -v163, v165, v165
	v_cvt_pk_bf16_f32 v254, v130, v131
	v_cvt_pk_bf16_f32 v255, v132, v133
	ds_write_b128 v211, v[252:255] offset:0
	s_waitcnt lgkmcnt(0)
	s_barrier
	s_branch .LBB1_13
